# sel tile head: running-max derived operands kept in registers and refreshed only on rescale, bias folded into one cndmask, diag test on scalar compare, last two K reads fill the cmp-to-cndmask gap
# speedup vs baseline: 1.0434x; 1.0087x over previous
; #define GAS __attribute__((address_space(1)))
; __device__ __forceinline__ unsigned pk4_fp8(float a, float b, float c, float d) { unsigned w = 0u; w = __builtin_amdgcn_cvt_pk_fp8_f32(a, b, w, false); w = __builtin_amdgcn_cvt_pk_fp8_f32(c, d, w, true); return w; }
; __device__ __forceinline__ void gs8_init(GS8& g, const bf16* qrow32) {
; #pragma unroll
;     for (int i = 0; i < 4; ++i) { const u32x4 w = *(const GAS u32x4*)(qrow32 + 8 * i);
;         g.q8[2 * i] = (int)pk4_fp8(bf_lo(w.x) * 8.f, bf_hi(w.x) * 8.f, bf_lo(w.y) * 8.f, bf_hi(w.y) * 8.f); g.q8[2 * i + 1] = (int)pk4_fp8(bf_lo(w.z) * 8.f, bf_hi(w.z) * 8.f, bf_lo(w.w) * 8.f, bf_hi(w.w) * 8.f); }
; #pragma unroll
;     for (int dt = 0; dt < 8; ++dt) g.o[dt] = (f32x4){0.f, 0.f, 0.f, 0.f};
;     g.m = -1e30f; g.l = 0.f;
; }
.LBB0_1782:
	s_cmp_lt_i32 s36, 1
	s_cbranch_scc1 .LBB0_1701
	s_waitcnt vmcnt(0)
	v_lshlrev_b32_e32 v34, 16, v0
	v_and_b32_e32 v0, 0xffff0000, v0
	v_mul_f32_e32 v34, 0x41000000, v34
	v_mul_f32_e32 v35, 0x41000000, v0
	v_mov_b32_e32 v0, v17
	v_cvt_pk_fp8_f32 v0, v34, v35
	v_lshlrev_b32_e32 v36, 16, v1
	v_and_b32_e32 v1, 0xffff0000, v1
	v_mul_f32_e32 v34, 0x41000000, v36
	v_mul_f32_e32 v1, 0x41000000, v1
	v_cvt_pk_fp8_f32 v0, v34, v1 op_sel:[0,0,1]
	v_lshlrev_b32_e32 v1, 16, v2
	v_mul_f32_e32 v34, 0x41000000, v1
	v_and_b32_e32 v1, 0xffff0000, v2
	v_mul_f32_e32 v2, 0x41000000, v1
	v_mov_b32_e32 v1, v17
	v_cvt_pk_fp8_f32 v1, v34, v2
	v_lshlrev_b32_e32 v35, 16, v3
	v_and_b32_e32 v3, 0xffff0000, v3
	v_mul_f32_e32 v2, 0x41000000, v35
	v_mul_f32_e32 v3, 0x41000000, v3
	v_cvt_pk_fp8_f32 v1, v2, v3 op_sel:[0,0,1]
	v_lshlrev_b32_e32 v2, 16, v30
	v_mul_f32_e32 v3, 0x41000000, v2
	v_and_b32_e32 v2, 0xffff0000, v30
	v_mul_f32_e32 v30, 0x41000000, v2
	v_mov_b32_e32 v2, v17
	v_cvt_pk_fp8_f32 v2, v3, v30
	v_lshlrev_b32_e32 v34, 16, v31
	v_and_b32_e32 v30, 0xffff0000, v31
	v_mul_f32_e32 v3, 0x41000000, v34
	v_mul_f32_e32 v30, 0x41000000, v30
	v_cvt_pk_fp8_f32 v2, v3, v30 op_sel:[0,0,1]
	v_lshlrev_b32_e32 v3, 16, v32
	v_mul_f32_e32 v30, 0x41000000, v3
	v_and_b32_e32 v3, 0xffff0000, v32
	v_mul_f32_e32 v31, 0x41000000, v3
	v_mov_b32_e32 v3, v17
	v_cvt_pk_fp8_f32 v3, v30, v31
	v_lshlrev_b32_e32 v32, 16, v33
	v_and_b32_e32 v31, 0xffff0000, v33
	v_mul_f32_e32 v30, 0x41000000, v32
	v_mul_f32_e32 v31, 0x41000000, v31
	v_cvt_pk_fp8_f32 v3, v30, v31 op_sel:[0,0,1]
	v_lshlrev_b32_e32 v30, 16, v4
	v_and_b32_e32 v4, 0xffff0000, v4
	v_mul_f32_e32 v30, 0x41000000, v30
	v_mul_f32_e32 v31, 0x41000000, v4
	v_mov_b32_e32 v4, v17
	v_cvt_pk_fp8_f32 v4, v30, v31
	v_lshlrev_b32_e32 v32, 16, v5
	v_and_b32_e32 v5, 0xffff0000, v5
	v_mul_f32_e32 v30, 0x41000000, v32
	v_mul_f32_e32 v5, 0x41000000, v5
	v_cvt_pk_fp8_f32 v4, v30, v5 op_sel:[0,0,1]
	v_lshlrev_b32_e32 v5, 16, v6
	v_mul_f32_e32 v30, 0x41000000, v5
	v_and_b32_e32 v5, 0xffff0000, v6
	v_mul_f32_e32 v6, 0x41000000, v5
	v_mov_b32_e32 v5, v17
	v_cvt_pk_fp8_f32 v5, v30, v6
	v_lshlrev_b32_e32 v31, 16, v7
	v_and_b32_e32 v7, 0xffff0000, v7
	v_mul_f32_e32 v6, 0x41000000, v31
	v_mul_f32_e32 v7, 0x41000000, v7
	v_cvt_pk_fp8_f32 v5, v6, v7 op_sel:[0,0,1]
	v_lshlrev_b32_e32 v6, 16, v26
	v_mul_f32_e32 v7, 0x41000000, v6
	v_and_b32_e32 v6, 0xffff0000, v26
	v_mul_f32_e32 v26, 0x41000000, v6
	v_mov_b32_e32 v6, v17
	v_cvt_pk_fp8_f32 v6, v7, v26
	v_lshlrev_b32_e32 v30, 16, v27
	v_and_b32_e32 v26, 0xffff0000, v27
	v_mul_f32_e32 v7, 0x41000000, v30
	v_mul_f32_e32 v26, 0x41000000, v26
	v_cvt_pk_fp8_f32 v6, v7, v26 op_sel:[0,0,1]
	v_lshlrev_b32_e32 v7, 16, v28
	v_mul_f32_e32 v26, 0x41000000, v7
	v_and_b32_e32 v7, 0xffff0000, v28
	v_mul_f32_e32 v27, 0x41000000, v7
	v_mov_b32_e32 v7, v17
	v_cvt_pk_fp8_f32 v7, v26, v27
	v_lshlrev_b32_e32 v28, 16, v29
	v_and_b32_e32 v27, 0xffff0000, v29
	v_mul_f32_e32 v26, 0x41000000, v28
	v_mul_f32_e32 v27, 0x41000000, v27
	v_cvt_pk_fp8_f32 v7, v26, v27 op_sel:[0,0,1]
	v_lshlrev_b32_e32 v26, 16, v8
	v_and_b32_e32 v8, 0xffff0000, v8
	v_mul_f32_e32 v26, 0x41000000, v26
	v_mul_f32_e32 v27, 0x41000000, v8
	v_mov_b32_e32 v8, v17
	v_cvt_pk_fp8_f32 v8, v26, v27
	v_lshlrev_b32_e32 v28, 16, v9
	v_and_b32_e32 v9, 0xffff0000, v9
	v_mul_f32_e32 v26, 0x41000000, v28
	v_mul_f32_e32 v9, 0x41000000, v9
	v_cvt_pk_fp8_f32 v8, v26, v9 op_sel:[0,0,1]
	v_lshlrev_b32_e32 v9, 16, v10
	v_mul_f32_e32 v26, 0x41000000, v9
	v_and_b32_e32 v9, 0xffff0000, v10
	v_mul_f32_e32 v10, 0x41000000, v9
	v_mov_b32_e32 v9, v17
	v_cvt_pk_fp8_f32 v9, v26, v10
	v_lshlrev_b32_e32 v27, 16, v11
	v_and_b32_e32 v11, 0xffff0000, v11
	v_mul_f32_e32 v10, 0x41000000, v27
	v_mul_f32_e32 v11, 0x41000000, v11
	v_cvt_pk_fp8_f32 v9, v10, v11 op_sel:[0,0,1]
	v_lshlrev_b32_e32 v10, 16, v22
	v_mul_f32_e32 v11, 0x41000000, v10
	v_and_b32_e32 v10, 0xffff0000, v22
	v_mul_f32_e32 v22, 0x41000000, v10
	v_mov_b32_e32 v10, v17
	v_cvt_pk_fp8_f32 v10, v11, v22
	v_lshlrev_b32_e32 v26, 16, v23
	v_and_b32_e32 v22, 0xffff0000, v23
	v_mul_f32_e32 v11, 0x41000000, v26
	v_mul_f32_e32 v22, 0x41000000, v22
	v_cvt_pk_fp8_f32 v10, v11, v22 op_sel:[0,0,1]
	v_lshlrev_b32_e32 v11, 16, v24
	v_mul_f32_e32 v22, 0x41000000, v11
; #define GAS __attribute__((address_space(1)))
; __device__ __forceinline__ unsigned pk4_fp8(float a, float b, float c, float d) { unsigned w = 0u; w = __builtin_amdgcn_cvt_pk_fp8_f32(a, b, w, false); w = __builtin_amdgcn_cvt_pk_fp8_f32(c, d, w, true); return w; }
; __device__ __forceinline__ void gs8_init(GS8& g, const bf16* qrow32) {
; #pragma unroll
;     for (int i = 0; i < 4; ++i) { const u32x4 w = *(const GAS u32x4*)(qrow32 + 8 * i);
;         g.q8[2 * i] = (int)pk4_fp8(bf_lo(w.x) * 8.f, bf_hi(w.x) * 8.f, bf_lo(w.y) * 8.f, bf_hi(w.y) * 8.f); g.q8[2 * i + 1] = (int)pk4_fp8(bf_lo(w.z) * 8.f, bf_hi(w.z) * 8.f, bf_lo(w.w) * 8.f, bf_hi(w.w) * 8.f); }
; #pragma unroll
;     for (int dt = 0; dt < 8; ++dt) g.o[dt] = (f32x4){0.f, 0.f, 0.f, 0.f};
;     g.m = -1e30f; g.l = 0.f;
; }
; __device__ __forceinline__ void mask_scores(f32x4 (&s)[4], int a, unsigned W, int kb, int q4) {
;     const float NEG = -__builtin_inff();
; #pragma unroll
;     for (int T_ = 0; T_ < 4; ++T_)
; #pragma unroll
;         for (int i = 0; i < 4; ++i) if ((unsigned)(a - (kb + 16 * T_ + 4 * q4 + i)) >= W) s[T_][i] = NEG;
; }
	v_and_b32_e32 v11, 0xffff0000, v24
	v_mul_f32_e32 v23, 0x41000000, v11
	v_mov_b32_e32 v11, v17
	v_cvt_pk_fp8_f32 v11, v22, v23
	v_lshlrev_b32_e32 v24, 16, v25
	v_and_b32_e32 v23, 0xffff0000, v25
	v_mul_f32_e32 v22, 0x41000000, v24
	v_mul_f32_e32 v23, 0x41000000, v23
	v_cvt_pk_fp8_f32 v11, v22, v23 op_sel:[0,0,1]
	v_lshlrev_b32_e32 v22, 16, v12
	v_and_b32_e32 v12, 0xffff0000, v12
	v_mul_f32_e32 v22, 0x41000000, v22
	v_mul_f32_e32 v23, 0x41000000, v12
	v_mov_b32_e32 v12, v17
	v_cvt_pk_fp8_f32 v12, v22, v23
	v_lshlrev_b32_e32 v24, 16, v13
	v_and_b32_e32 v13, 0xffff0000, v13
	v_mul_f32_e32 v22, 0x41000000, v24
	v_mul_f32_e32 v13, 0x41000000, v13
	v_cvt_pk_fp8_f32 v12, v22, v13 op_sel:[0,0,1]
	v_lshlrev_b32_e32 v13, 16, v14
	v_mul_f32_e32 v22, 0x41000000, v13
	v_and_b32_e32 v13, 0xffff0000, v14
	v_mul_f32_e32 v14, 0x41000000, v13
	v_mov_b32_e32 v13, v17
	v_cvt_pk_fp8_f32 v13, v22, v14
	v_lshlrev_b32_e32 v23, 16, v15
	v_and_b32_e32 v15, 0xffff0000, v15
	v_mul_f32_e32 v14, 0x41000000, v23
	v_mul_f32_e32 v15, 0x41000000, v15
	v_cvt_pk_fp8_f32 v13, v14, v15 op_sel:[0,0,1]
	v_lshlrev_b32_e32 v14, 16, v18
	v_mul_f32_e32 v15, 0x41000000, v14
	v_and_b32_e32 v14, 0xffff0000, v18
	v_mul_f32_e32 v18, 0x41000000, v14
	v_mov_b32_e32 v14, v17
	v_cvt_pk_fp8_f32 v14, v15, v18
	v_lshlrev_b32_e32 v22, 16, v19
	v_and_b32_e32 v18, 0xffff0000, v19
	v_mul_f32_e32 v15, 0x41000000, v22
	v_mul_f32_e32 v18, 0x41000000, v18
	v_cvt_pk_fp8_f32 v14, v15, v18 op_sel:[0,0,1]
	v_lshlrev_b32_e32 v15, 16, v20
	v_mul_f32_e32 v18, 0x41000000, v15
	v_and_b32_e32 v15, 0xffff0000, v20
	v_mul_f32_e32 v19, 0x41000000, v15
	v_mov_b32_e32 v15, v17
	v_cvt_pk_fp8_f32 v15, v18, v19
	v_lshlrev_b32_e32 v20, 16, v21
	v_and_b32_e32 v19, 0xffff0000, v21
	v_mul_f32_e32 v18, 0x41000000, v20
	v_mul_f32_e32 v19, 0x41000000, v19
	v_cvt_pk_fp8_f32 v15, v18, v19 op_sel:[0,0,1]
	v_mov_b32_e32 v52, v17
	v_mov_b32_e32 v53, v17
	v_mov_b32_e32 v54, v17
	v_mov_b32_e32 v55, v17
	v_mov_b64_e32 v[58:59], v[54:55]
	v_mov_b64_e32 v[62:63], v[54:55]
	v_mov_b64_e32 v[66:67], v[54:55]
	v_mov_b64_e32 v[70:71], v[54:55]
	v_mov_b64_e32 v[74:75], v[54:55]
	v_mov_b64_e32 v[78:79], v[54:55]
	v_mov_b64_e32 v[82:83], v[54:55]
	v_mov_b64_e32 v[20:21], v[52:53]
	v_mov_b64_e32 v[24:25], v[52:53]
	v_mov_b64_e32 v[28:29], v[52:53]
	v_mov_b64_e32 v[32:33], v[52:53]
	v_mov_b64_e32 v[36:37], v[52:53]
	v_mov_b64_e32 v[40:41], v[52:53]
	v_mov_b64_e32 v[44:45], v[52:53]
	v_mov_b64_e32 v[48:49], v[52:53]
	v_add_u32_e32 v184, -2, v16
	v_add_u32_e32 v185, -3, v16
	s_add_i32 s68, s55, -16
	v_subrev_u32_e32 v186, 17, v16
	v_subrev_u32_e32 v187, 18, v16
	v_subrev_u32_e32 v188, 19, v16
	s_sub_i32 s69, s55, 32
	v_subrev_u32_e32 v189, 33, v16
	v_subrev_u32_e32 v190, 34, v16
	v_subrev_u32_e32 v191, 35, v16
	s_sub_i32 s70, s55, 48
	v_subrev_u32_e32 v192, 49, v16
	v_subrev_u32_e32 v193, 50, v16
	v_subrev_u32_e32 v194, 51, v16
	v_or_b32_e32 v195, 4, v16
	v_add_u32_e32 v196, 2, v16
	v_add_u32_e32 v197, 1, v16
	s_add_i32 s71, s55, -12
	v_add_u32_e32 v198, -13, v16
	v_add_u32_e32 v199, -14, v16
	v_add_u32_e32 v200, -15, v16
	s_sub_i32 s72, s55, 28
	v_subrev_u32_e32 v201, 29, v16
	v_subrev_u32_e32 v202, 30, v16
	v_subrev_u32_e32 v203, 31, v16
	s_sub_i32 s73, s55, 44
	v_subrev_u32_e32 v204, 45, v16
	v_subrev_u32_e32 v205, 46, v16
	v_subrev_u32_e32 v206, 47, v16
	s_max_i32 s89, s59, 1
	s_mov_b32 s36, 0
	v_mov_b32_e32 v19, 0xf149f2ca
	v_mov_b32_e32 v183, 0
	v_mov_b64_e32 v[56:57], v[52:53]
	v_mov_b64_e32 v[60:61], v[52:53]
	v_mov_b64_e32 v[64:65], v[52:53]
	v_mov_b64_e32 v[68:69], v[52:53]
	v_mov_b64_e32 v[72:73], v[52:53]
	v_mov_b64_e32 v[76:77], v[52:53]
	v_mov_b64_e32 v[80:81], v[52:53]
	v_mov_b32_e32 v182, 0
	v_mov_b32_e32 v117, 0xf149f2ca
	v_mov_b32_e32 v216, 0x40a00000
	v_mov_b32_e32 v217, 0xc0a00000
	v_mov_b32_e32 v218, 0xf149f2ca
	v_mov_b32_e32 v219, 0
	v_mov_b32_e32 v220, 0x40a00000
	v_mov_b32_e32 v221, 0xc0a00000
	v_mov_b32_e32 v222, 0xf149f2ca
	v_mov_b32_e32 v223, 0
	v_mov_b64_e32 v[22:23], v[54:55]
	v_mov_b64_e32 v[26:27], v[54:55]
	v_mov_b64_e32 v[30:31], v[54:55]
	v_mov_b64_e32 v[34:35], v[54:55]
	v_mov_b64_e32 v[38:39], v[54:55]
	v_mov_b64_e32 v[42:43], v[54:55]
	v_mov_b64_e32 v[46:47], v[54:55]
	v_mov_b64_e32 v[50:51], v[54:55]

; __device__ __forceinline__ float xmax16(float v) { float a = v, b = v; PL_SWAP16(a, b); return fmaxf(a, b); }
; __device__ __forceinline__ float xmax32(float v) { float a = v, b = v; PL_SWAP32(a, b); return fmaxf(a, b); }
; __device__ __forceinline__ unsigned lds_addr(const LAS void* p) { return (unsigned)(size_t)p; }
; template <class G> __device__ __forceinline__ void online_sm8(f32x4 (&s)[4], G& g, const float ref) {
;     float mx = s[0][0];
; #pragma unroll
;     for (int T_ = 0; T_ < 4; ++T_)
; #pragma unroll
;         for (int i = 0; i < 4; ++i) mx = fmaxf(mx, s[T_][i]);
;     const float t = mx + (ref - 5.f);
;     if (!__all(t <= g.m + SM_THR8)) {
;         const float mr = xmax32(xmax16(t));
;         const float mn = fmaxf(g.m, mr); const float al = __builtin_amdgcn_exp2f(g.m - mn); g.m = mn; g.l *= al;
; #pragma unroll
;         for (int dt = 0; dt < 8; ++dt) g.o[dt] = g.o[dt] * al;
;         const float d = ref - mn;
; #pragma unroll
;         for (int T_ = 0; T_ < 4; ++T_)
; #pragma unroll
;             for (int i = 0; i < 4; ++i) s[T_][i] += d;
;     }
; template <bool DUMMY> __device__ __forceinline__ void sel_phase(Frame& F) {
;     ...
;                 const unsigned a0 = byte & 0xfu, a1 = byte >> 4;
;                 if (byte == 0u) continue;
;                 const bool selA = ((a0 >> (c >> 2)) & 1u) != 0u, selB = ((a1 >> (c >> 2)) & 1u) != 0u;
;                 const float NINF = -__builtin_inff();
;                 const int kb = jc * 64; const bool diag = (jc == cur); f32x4 s0[4], s1[4];
;                 const float bA = selA ? 0.f : NINF, bB = selB ? 0.f : NINF;
;                 if (a0 != 0u) {
;                     const float rf = sm8_ref(g0);
;                     VT8Frag vf; qk8_tile_c(s0, g0, lds_addr(sb) + (unsigned)klane, bA + (5.f - rf)); pv8_issue(vf, lds_addr(sb + K8TB) + (unsigned)vtlane);
;                     if (diag) mask_scores(s0, tokA, 0x40000000u, kb, kq);
;                     online_sm8(s0, g0, rf);
.Lsel_nodma:
	s_lshr_b32 s45, s67, s36
	s_and_b32 s97, s45, 0xff
	s_cbranch_scc0 .LBB0_1798
	ds_read_b128 v[84:87], v208 offset:0
	ds_read_b128 v[88:91], v208 offset:16
	ds_read_b128 v[92:95], v208 offset:0x900
	ds_read_b128 v[96:99], v208 offset:0x910
	ds_read_b128 v[118:121], v208 offset:0x1200
	ds_read_b128 v[122:125], v208 offset:0x1210
	s_lshr_b32 s44, s66, s36
	s_and_b32 s44, s44, 0xff
	s_and_b32 vcc_lo, s45, 15
	s_cbranch_scc0 .Lsel_g1_pre
	v_and_b32_e32 v18, s45, v154
	v_cmp_eq_u32_e32 vcc, 0, v18
	ds_read_b128 v[126:129], v208 offset:0x1b00
	ds_read_b128 v[130:133], v208 offset:0x1b10
	v_cndmask_b32_e32 v210, v216, v181, vcc
	v_mov_b32_e32 v211, v210
	v_mov_b32_e32 v212, v210
	v_mov_b32_e32 v213, v210
	s_waitcnt lgkmcnt(6)
	s_nop 1
	v_mfma_scale_f32_16x16x128_f8f6f4 v[84:87], v[84:91], v[0:7], v[210:213], v178, v177 op_sel_hi:[0,0,0]
	ds_read_b64 v[148:149], v207 offset:0
	ds_read_b64 v[146:147], v207 offset:32
	ds_read_b64 v[144:145], v207 offset:0x500
	ds_read_b64 v[142:143], v207 offset:0x520
	ds_read_b64 v[140:141], v207 offset:0xa00
	ds_read_b64 v[136:137], v207 offset:0xa20
	ds_read_b64 v[138:139], v207 offset:0xf00
	ds_read_b64 v[134:135], v207 offset:0xf20
	s_waitcnt lgkmcnt(12)
	v_mfma_scale_f32_16x16x128_f8f6f4 v[88:91], v[92:99], v[0:7], v[210:213], v178, v177 op_sel_hi:[0,0,0]
	s_waitcnt lgkmcnt(10)
	v_mfma_scale_f32_16x16x128_f8f6f4 v[92:95], v[118:125], v[0:7], v[210:213], v178, v177 op_sel_hi:[0,0,0]
	s_waitcnt lgkmcnt(8)
	v_mfma_scale_f32_16x16x128_f8f6f4 v[96:99], v[126:133], v[0:7], v[210:213], v178, v177 op_sel_hi:[0,0,0]
	ds_read_b64 v[132:133], v207 offset:0x1400
	ds_read_b64 v[130:131], v207 offset:0x1420
	ds_read_b64 v[128:129], v207 offset:0x1900
	ds_read_b64 v[126:127], v207 offset:0x1920
	ds_read_b64 v[124:125], v207 offset:0x1e00
	ds_read_b64 v[120:121], v207 offset:0x1e20
	ds_read_b64 v[118:119], v207 offset:0x2300
	ds_read_b64 v[122:123], v207 offset:0x2320
	s_cmp_eq_u32 s44, s58
	s_cbranch_scc0 .LBB0_1806
	s_lshl_b32 s12, s44, 6
	v_add_u32_e32 v18, s12, v155
	v_sub_u32_e32 v114, s55, v18
	v_cmp_gt_u32_e32 vcc, 2.0, v114
	v_sub_u32_e32 v114, v18, v16
	s_nop 2
	v_cndmask_b32_e32 v84, v181, v84, vcc
	v_cmp_lt_u32_e32 vcc, s91, v114
	v_sub_u32_e32 v114, v184, v18
	s_nop 0
	v_cndmask_b32_e32 v85, v181, v85, vcc
	v_cmp_gt_u32_e32 vcc, 2.0, v114
	v_sub_u32_e32 v114, v185, v18
	s_nop 0
	v_cndmask_b32_e32 v86, v181, v86, vcc
	v_cmp_gt_u32_e32 vcc, 2.0, v114
	v_sub_u32_e32 v114, s68, v18
	s_nop 0
	v_cndmask_b32_e32 v87, v181, v87, vcc
	v_cmp_gt_u32_e32 vcc, 2.0, v114
	v_sub_u32_e32 v114, v186, v18
	s_nop 0
	v_cndmask_b32_e32 v88, v181, v88, vcc
	v_cmp_gt_u32_e32 vcc, 2.0, v114
	v_sub_u32_e32 v114, v187, v18
	s_nop 0
	v_cndmask_b32_e32 v89, v181, v89, vcc
	v_cmp_gt_u32_e32 vcc, 2.0, v114
	v_sub_u32_e32 v114, v188, v18
	s_nop 0
	v_cndmask_b32_e32 v90, v181, v90, vcc
	v_cmp_gt_u32_e32 vcc, 2.0, v114
	v_sub_u32_e32 v114, s69, v18
	s_nop 0
	v_cndmask_b32_e32 v91, v181, v91, vcc
	v_cmp_gt_u32_e32 vcc, 2.0, v114
	v_sub_u32_e32 v114, v189, v18
	s_nop 0
	v_cndmask_b32_e32 v92, v181, v92, vcc
	v_cmp_gt_u32_e32 vcc, 2.0, v114
	v_sub_u32_e32 v114, v190, v18
	s_nop 0
	v_cndmask_b32_e32 v93, v181, v93, vcc
	v_cmp_gt_u32_e32 vcc, 2.0, v114
	v_sub_u32_e32 v114, v191, v18
	s_nop 0
	v_cndmask_b32_e32 v94, v181, v94, vcc
	v_cmp_gt_u32_e32 vcc, 2.0, v114
	v_sub_u32_e32 v114, s70, v18
	s_nop 0
	v_cndmask_b32_e32 v95, v181, v95, vcc
	v_cmp_gt_u32_e32 vcc, 2.0, v114
	v_sub_u32_e32 v114, v192, v18
	s_nop 0
	v_cndmask_b32_e32 v96, v181, v96, vcc
	v_cmp_gt_u32_e32 vcc, 2.0, v114
	v_sub_u32_e32 v114, v193, v18
	v_sub_u32_e32 v18, v194, v18
	v_cndmask_b32_e32 v97, v181, v97, vcc
	v_cmp_gt_u32_e32 vcc, 2.0, v114
	s_nop 1
	v_cndmask_b32_e32 v98, v181, v98, vcc
	v_cmp_gt_u32_e32 vcc, 2.0, v18
	s_nop 1
	v_cndmask_b32_e32 v99, v181, v99, vcc
.LBB0_1806:
	v_max_f32_e32 v18, v84, v85
	v_max3_f32 v18, v18, v86, v87
	v_max3_f32 v18, v18, v88, v89
	v_max3_f32 v18, v18, v90, v91
	v_max3_f32 v18, v18, v92, v93
	v_max3_f32 v18, v18, v94, v95
	v_max3_f32 v18, v18, v96, v97
	v_max3_f32 v114, v18, v98, v99
	v_add_f32_e32 v150, v217, v114
	v_cmp_le_f32_e32 vcc, v150, v218
	s_cmp_eq_u64 vcc, exec
	s_cbranch_scc1 .LBB0_1808
	v_mov_b32_e32 v18, v84
	v_mov_b32_e32 v84, v150
	s_nop 1
	v_permlane16_swap_b32 v84, v150
	v_mov_b32_e32 v151, v96
	v_max_f32_e32 v114, v150, v150
	v_max_f32_e32 v84, v84, v84
	v_max_f32_e32 v84, v84, v114
	v_mov_b32_e32 v114, v84
	s_nop 1
	v_permlane32_swap_b32 v114, v84
	v_mov_b32_e32 v150, v92
	v_max3_f32 v114, v19, v114, v84
	v_sub_f32_e32 v19, v19, v114
	v_exp_f32_e32 v84, v19
	v_mov_b32_e32 v19, v88
	v_mov_b32_e32 v210, v85
	v_mov_b32_e32 v211, v86
	v_mul_f32_e32 v183, v183, v84
	v_pk_mul_f32 v[82:83], v[82:83], v[84:85] op_sel_hi:[1,0]
	v_pk_mul_f32 v[80:81], v[80:81], v[84:85] op_sel_hi:[1,0]
	v_pk_mul_f32 v[78:79], v[78:79], v[84:85] op_sel_hi:[1,0]
	v_pk_mul_f32 v[76:77], v[76:77], v[84:85] op_sel_hi:[1,0]
	v_pk_mul_f32 v[74:75], v[74:75], v[84:85] op_sel_hi:[1,0]
	v_pk_mul_f32 v[72:73], v[72:73], v[84:85] op_sel_hi:[1,0]
	v_pk_mul_f32 v[70:71], v[70:71], v[84:85] op_sel_hi:[1,0]
	v_pk_mul_f32 v[68:69], v[68:69], v[84:85] op_sel_hi:[1,0]
	v_pk_mul_f32 v[66:67], v[66:67], v[84:85] op_sel_hi:[1,0]
	v_pk_mul_f32 v[64:65], v[64:65], v[84:85] op_sel_hi:[1,0]
	v_pk_mul_f32 v[62:63], v[62:63], v[84:85] op_sel_hi:[1,0]
	v_pk_mul_f32 v[60:61], v[60:61], v[84:85] op_sel_hi:[1,0]
	v_pk_mul_f32 v[58:59], v[58:59], v[84:85] op_sel_hi:[1,0]
	v_pk_mul_f32 v[56:57], v[56:57], v[84:85] op_sel_hi:[1,0]
	v_pk_mul_f32 v[54:55], v[54:55], v[84:85] op_sel_hi:[1,0]
	v_pk_mul_f32 v[52:53], v[52:53], v[84:85] op_sel_hi:[1,0]
	v_sub_f32_e32 v84, v219, v114
	v_pk_add_f32 v[212:213], v[18:19], v[84:85] op_sel_hi:[1,0]
	v_mov_b32_e32 v18, v89
	v_mov_b32_e32 v19, v90
	v_pk_add_f32 v[214:215], v[18:19], v[84:85] op_sel_hi:[1,0]
	v_mov_b32_e32 v18, v93
	v_mov_b32_e32 v19, v94
	v_pk_add_f32 v[88:89], v[18:19], v[84:85] op_sel_hi:[1,0]
	v_mov_b32_e32 v18, v97
	v_mov_b32_e32 v19, v98
	v_pk_add_f32 v[210:211], v[210:211], v[84:85] op_sel_hi:[1,0]
	v_pk_add_f32 v[150:151], v[150:151], v[84:85] op_sel_hi:[1,0]
	v_pk_add_f32 v[92:93], v[18:19], v[84:85] op_sel_hi:[1,0]
	v_add_f32_e32 v87, v87, v84
	v_add_f32_e32 v91, v91, v84
	v_add_f32_e32 v95, v95, v84
	v_add_f32_e32 v99, v99, v84
	v_mov_b32_e32 v19, v114
	v_cmp_ngt_f32_e32 vcc, s90, v19
	v_mov_b32_e32 v97, v92
	v_mov_b32_e32 v98, v93
	v_mov_b32_e32 v93, v88
	v_mov_b32_e32 v94, v89
	v_mov_b32_e32 v89, v214
	v_mov_b32_e32 v90, v215
	v_mov_b32_e32 v85, v210
	v_mov_b32_e32 v86, v211
	v_mov_b32_e32 v84, v212
	v_mov_b32_e32 v88, v213
	v_mov_b32_e32 v92, v150
	v_mov_b32_e32 v96, v151
	v_cndmask_b32_e32 v219, 0, v19, vcc
	v_add_f32_e32 v218, v19, v115
	v_sub_f32_e32 v216, 0x40a00000, v219
	v_add_f32_e32 v217, 0xc0a00000, v219

; __device__ __forceinline__ float xmax16(float v) { float a = v, b = v; PL_SWAP16(a, b); return fmaxf(a, b); }
; __device__ __forceinline__ float xmax32(float v) { float a = v, b = v; PL_SWAP32(a, b); return fmaxf(a, b); }
; __device__ __forceinline__ unsigned lds_addr(const LAS void* p) { return (unsigned)(size_t)p; }
; template <class G> __device__ __forceinline__ void online_sm8(f32x4 (&s)[4], G& g, const float ref) {
;     float mx = s[0][0];
; #pragma unroll
;     for (int T_ = 0; T_ < 4; ++T_)
; #pragma unroll
;         for (int i = 0; i < 4; ++i) mx = fmaxf(mx, s[T_][i]);
;     const float t = mx + (ref - 5.f);
;     if (!__all(t <= g.m + SM_THR8)) {
;         const float mr = xmax32(xmax16(t));
;         const float mn = fmaxf(g.m, mr); const float al = __builtin_amdgcn_exp2f(g.m - mn); g.m = mn; g.l *= al;
; #pragma unroll
;         for (int dt = 0; dt < 8; ++dt) g.o[dt] = g.o[dt] * al;
;         const float d = ref - mn;
; #pragma unroll
;         for (int T_ = 0; T_ < 4; ++T_)
; #pragma unroll
;             for (int i = 0; i < 4; ++i) s[T_][i] += d;
;     }
; template <bool DUMMY> __device__ __forceinline__ void sel_phase(Frame& F) {
;     ...
;                 if (a1 != 0u) {
;                     const float rf = sm8_ref(g1);
;                     VT8Frag vf; qk8_tile_c(s0, g1, lds_addr(sb) + (unsigned)klane, bB + (5.f - rf)); pv8_issue(vf, lds_addr(sb + K8TB) + (unsigned)vtlane);
;                     if (diag) mask_scores(s0, tokA + 4, 0x40000000u, kb, kq);
;                     online_sm8(s0, g1, rf);
;                     pv8_mm(g1, s0, vf);
.Lsel_g1_pre:
	s_lshr_b32 s45, s45, 4
	v_and_b32_e32 v18, s45, v154
	v_cmp_eq_u32_e32 vcc, 0, v18
	ds_read_b128 v[126:129], v208 offset:0x1b00
	ds_read_b128 v[130:133], v208 offset:0x1b10
	v_cndmask_b32_e32 v210, v220, v181, vcc
	v_mov_b32_e32 v211, v210
	v_mov_b32_e32 v212, v210
	v_mov_b32_e32 v213, v210
	s_waitcnt lgkmcnt(6)
	s_nop 1
	v_mfma_scale_f32_16x16x128_f8f6f4 v[84:87], v[84:91], v[8:15], v[210:213], v178, v177 op_sel_hi:[0,0,0]
	ds_read_b64 v[148:149], v207 offset:0
	ds_read_b64 v[146:147], v207 offset:32
	ds_read_b64 v[144:145], v207 offset:0x500
	ds_read_b64 v[142:143], v207 offset:0x520
	ds_read_b64 v[140:141], v207 offset:0xa00
	ds_read_b64 v[136:137], v207 offset:0xa20
	ds_read_b64 v[138:139], v207 offset:0xf00
	ds_read_b64 v[134:135], v207 offset:0xf20
	s_waitcnt lgkmcnt(12)
	v_mfma_scale_f32_16x16x128_f8f6f4 v[88:91], v[92:99], v[8:15], v[210:213], v178, v177 op_sel_hi:[0,0,0]
	s_waitcnt lgkmcnt(10)
	v_mfma_scale_f32_16x16x128_f8f6f4 v[92:95], v[118:125], v[8:15], v[210:213], v178, v177 op_sel_hi:[0,0,0]
	s_waitcnt lgkmcnt(8)
	v_mfma_scale_f32_16x16x128_f8f6f4 v[96:99], v[126:133], v[8:15], v[210:213], v178, v177 op_sel_hi:[0,0,0]
	ds_read_b64 v[132:133], v207 offset:0x1400
	ds_read_b64 v[130:131], v207 offset:0x1420
	ds_read_b64 v[128:129], v207 offset:0x1900
	ds_read_b64 v[126:127], v207 offset:0x1920
	ds_read_b64 v[124:125], v207 offset:0x1e00
	ds_read_b64 v[120:121], v207 offset:0x1e20
	ds_read_b64 v[118:119], v207 offset:0x2300
	ds_read_b64 v[122:123], v207 offset:0x2320
	s_cmp_eq_u32 s44, s58
	s_cbranch_scc0 .LBB0_1812
	s_lshl_b32 s12, s44, 6
	v_add_u32_e32 v114, s12, v155
	v_sub_u32_e32 v116, v195, v114
	v_cmp_gt_u32_e32 vcc, 2.0, v116
	v_sub_u32_e32 v116, v114, v195
	s_nop 2
	v_cndmask_b32_e32 v84, v181, v84, vcc
	v_cmp_lt_u32_e32 vcc, s91, v116
	v_sub_u32_e32 v116, v196, v114
	s_nop 0
	v_cndmask_b32_e32 v85, v181, v85, vcc
	v_cmp_gt_u32_e32 vcc, 2.0, v116
	v_sub_u32_e32 v116, v197, v114
	s_nop 0
	v_cndmask_b32_e32 v86, v181, v86, vcc
	v_cmp_gt_u32_e32 vcc, 2.0, v116
	v_sub_u32_e32 v116, s71, v114
	s_nop 0
	v_cndmask_b32_e32 v87, v181, v87, vcc
	v_cmp_gt_u32_e32 vcc, 2.0, v116
	v_sub_u32_e32 v116, v198, v114
	s_nop 0
	v_cndmask_b32_e32 v88, v181, v88, vcc
	v_cmp_gt_u32_e32 vcc, 2.0, v116
	v_sub_u32_e32 v116, v199, v114
	s_nop 0
	v_cndmask_b32_e32 v89, v181, v89, vcc
	v_cmp_gt_u32_e32 vcc, 2.0, v116
	v_sub_u32_e32 v116, v200, v114
	s_nop 0
	v_cndmask_b32_e32 v90, v181, v90, vcc
	v_cmp_gt_u32_e32 vcc, 2.0, v116
	v_sub_u32_e32 v116, s72, v114
	s_nop 0
	v_cndmask_b32_e32 v91, v181, v91, vcc
	v_cmp_gt_u32_e32 vcc, 2.0, v116
	v_sub_u32_e32 v116, v201, v114
	s_nop 0
	v_cndmask_b32_e32 v92, v181, v92, vcc
	v_cmp_gt_u32_e32 vcc, 2.0, v116
	v_sub_u32_e32 v116, v202, v114
	s_nop 0
	v_cndmask_b32_e32 v93, v181, v93, vcc
	v_cmp_gt_u32_e32 vcc, 2.0, v116
	v_sub_u32_e32 v116, v203, v114
	s_nop 0
	v_cndmask_b32_e32 v94, v181, v94, vcc
	v_cmp_gt_u32_e32 vcc, 2.0, v116
	v_sub_u32_e32 v116, s73, v114
	s_nop 0
	v_cndmask_b32_e32 v95, v181, v95, vcc
	v_cmp_gt_u32_e32 vcc, 2.0, v116
	v_sub_u32_e32 v116, v204, v114
	s_nop 0
	v_cndmask_b32_e32 v96, v181, v96, vcc
	v_cmp_gt_u32_e32 vcc, 2.0, v116
	v_sub_u32_e32 v116, v205, v114
	v_sub_u32_e32 v114, v206, v114
	v_cndmask_b32_e32 v97, v181, v97, vcc
	v_cmp_gt_u32_e32 vcc, 2.0, v116
	s_nop 1
	v_cndmask_b32_e32 v98, v181, v98, vcc
	v_cmp_gt_u32_e32 vcc, 2.0, v114
	s_nop 1
	v_cndmask_b32_e32 v99, v181, v99, vcc
.LBB0_1812:
	v_max_f32_e32 v114, v84, v85
	v_max3_f32 v114, v114, v86, v87
	v_max3_f32 v114, v114, v88, v89
	v_max3_f32 v114, v114, v90, v91
	v_max3_f32 v114, v114, v92, v93
	v_max3_f32 v114, v114, v94, v95
	v_max3_f32 v114, v114, v96, v97
	v_max3_f32 v114, v114, v98, v99
	v_add_f32_e32 v150, v221, v114
	v_cmp_le_f32_e32 vcc, v150, v222
	s_cmp_eq_u64 vcc, exec
	s_cbranch_scc1 .LBB0_1797
	v_mov_b32_e32 v116, v84
	v_mov_b32_e32 v84, v150
	s_nop 1
	v_permlane16_swap_b32 v150, v84
	v_mov_b32_e32 v151, v96
	v_max_f32_e32 v84, v84, v84
	v_max_f32_e32 v114, v150, v150
	v_max_f32_e32 v84, v114, v84
	v_mov_b32_e32 v114, v84
	s_nop 1
	v_permlane32_swap_b32 v84, v114
	v_mov_b32_e32 v150, v92
	v_max3_f32 v114, v117, v84, v114
	v_sub_f32_e32 v84, v117, v114
	v_exp_f32_e32 v84, v84
	v_sub_f32_e32 v18, v223, v114
	v_mov_b32_e32 v117, v88
	v_mov_b32_e32 v88, v93
	v_mul_f32_e32 v182, v182, v84
	v_pk_mul_f32 v[50:51], v[50:51], v[84:85] op_sel_hi:[1,0]
	v_pk_mul_f32 v[48:49], v[48:49], v[84:85] op_sel_hi:[1,0]
	v_pk_mul_f32 v[46:47], v[46:47], v[84:85] op_sel_hi:[1,0]
	v_pk_mul_f32 v[44:45], v[44:45], v[84:85] op_sel_hi:[1,0]
	v_pk_mul_f32 v[42:43], v[42:43], v[84:85] op_sel_hi:[1,0]
	v_pk_mul_f32 v[40:41], v[40:41], v[84:85] op_sel_hi:[1,0]
	v_pk_mul_f32 v[38:39], v[38:39], v[84:85] op_sel_hi:[1,0]
	v_pk_mul_f32 v[36:37], v[36:37], v[84:85] op_sel_hi:[1,0]
	v_pk_mul_f32 v[34:35], v[34:35], v[84:85] op_sel_hi:[1,0]
	v_pk_mul_f32 v[32:33], v[32:33], v[84:85] op_sel_hi:[1,0]
	v_pk_mul_f32 v[30:31], v[30:31], v[84:85] op_sel_hi:[1,0]
	v_pk_mul_f32 v[28:29], v[28:29], v[84:85] op_sel_hi:[1,0]
	v_pk_mul_f32 v[26:27], v[26:27], v[84:85] op_sel_hi:[1,0]
	v_pk_mul_f32 v[24:25], v[24:25], v[84:85] op_sel_hi:[1,0]
	v_pk_mul_f32 v[22:23], v[22:23], v[84:85] op_sel_hi:[1,0]
	v_pk_mul_f32 v[20:21], v[20:21], v[84:85] op_sel_hi:[1,0]
	v_mov_b32_e32 v84, v85
	v_mov_b32_e32 v85, v86
	v_pk_add_f32 v[210:211], v[84:85], v[18:19] op_sel_hi:[1,0]
	v_mov_b32_e32 v84, v89
	v_mov_b32_e32 v85, v90
	v_mov_b32_e32 v89, v94
	v_mov_b32_e32 v92, v97
	v_mov_b32_e32 v93, v98
	v_pk_add_f32 v[212:213], v[116:117], v[18:19] op_sel_hi:[1,0]
	v_pk_add_f32 v[84:85], v[84:85], v[18:19] op_sel_hi:[1,0]
	v_pk_add_f32 v[88:89], v[88:89], v[18:19] op_sel_hi:[1,0]
	v_pk_add_f32 v[150:151], v[150:151], v[18:19] op_sel_hi:[1,0]
	v_pk_add_f32 v[92:93], v[92:93], v[18:19] op_sel_hi:[1,0]
	v_add_f32_e32 v87, v87, v18
	v_add_f32_e32 v91, v91, v18
	v_add_f32_e32 v95, v95, v18
	v_add_f32_e32 v99, v99, v18
	v_mov_b32_e32 v117, v114
	v_cmp_ngt_f32_e32 vcc, s90, v117
	v_mov_b32_e32 v97, v92
	v_mov_b32_e32 v98, v93
	v_mov_b32_e32 v93, v88
	v_mov_b32_e32 v94, v89
	v_mov_b32_e32 v89, v84
	v_mov_b32_e32 v90, v85
	v_mov_b32_e32 v85, v210
	v_mov_b32_e32 v86, v211
	v_mov_b32_e32 v84, v212
	v_mov_b32_e32 v88, v213
	v_mov_b32_e32 v92, v150
	v_mov_b32_e32 v96, v151
	v_cndmask_b32_e32 v223, 0, v117, vcc
	v_add_f32_e32 v222, v117, v115
	v_sub_f32_e32 v220, 0x40a00000, v223
	v_add_f32_e32 v221, 0xc0a00000, v223
	s_branch .LBB0_1797
